# stack5: stack4 plus HID pass bias fetch issued with the partial loads and counted waits
# speedup vs baseline: 1.0159x; 1.0045x over previous
; __device__ __forceinline__ unsigned cvtpk(float lo, float hi) { unsigned r; asm volatile("v_cvt_pk_bf16_f32 %0, %1, %2" : "=v"(r) : "v"(lo), "v"(hi)); return r; }
; __global__ void __launch_bounds__(512, 2) fwd(Args args) {
;     ...
;                 for (int i = bx * 512 + tid; i < 4096 * 128; i += G * 512) { const int row = i >> 7, cq = (i & 127) * 4; const size_t o = (size_t)row * 512 + cq;
;                     const f32x4 a = *(const f32x4*)(P + o), b = *(const f32x4*)(P + (size_t)4096 * 512 + o), c = *(const f32x4*)(P + (size_t)2 * 4096 * 512 + o), d = *(const f32x4*)(P + (size_t)3 * 4096 * 512 + o);
;                     const f32x4 s = ((a + b) + (c + d)) + *(const f32x4*)(bias + (row >> 11) * 512 + cq);
;                     u32x2 w; w.x = cvtpk(pg8::gelu_tanh(s[0]), pg8::gelu_tanh(s[1])); w.y = cvtpk(pg8::gelu_tanh(s[2]), pg8::gelu_tanh(s[3])); *(u32x2*)(hid + o) = w; }
.LBB0_2210:
	v_ashrrev_i32_e32 v4, 7, v0
	v_ashrrev_i32_e32 v5, 31, v4
	v_and_b32_e32 v2, 0x1fc, v1
	v_lshlrev_b64 v[20:21], 9, v[4:5]
	v_or_b32_e32 v20, v20, v2
	v_lshlrev_b64 v[16:17], 2, v[20:21]
	v_lshl_add_u64 v[4:5], s[6:7], 0, v[16:17]
	v_lshl_add_u64 v[8:9], s[10:11], 0, v[16:17]
	s_waitcnt lgkmcnt(0)
	v_lshl_add_u64 v[12:13], s[12:13], 0, v[16:17]
	v_lshl_add_u64 v[16:17], s[14:15], 0, v[16:17]
	global_load_dwordx4 v[4:7], v[4:5], off
	v_lshlrev_b32_e32 v2, 2, v2
	global_load_dwordx4 v[8:11], v[8:9], off
	s_mov_b32 s0, 0x7ffff
	global_load_dwordx4 v[12:15], v[12:13], off
	v_add_u32_e32 v1, s19, v1
	global_load_dwordx4 v[16:19], v[16:17], off
	v_ashrrev_i32_e32 v26, 9, v0
	v_and_b32_e32 v26, 0xfffffe00, v26
	v_ashrrev_i32_e32 v27, 31, v26
	v_lshl_add_u64 v[26:27], v[26:27], 2, s[8:9]
	v_lshl_add_u64 v[26:27], v[26:27], 0, v[2:3]
	global_load_dwordx4 v[22:25], v[26:27], off
	s_waitcnt vmcnt(3)
	v_pk_add_f32 v[6:7], v[6:7], v[10:11]
	v_pk_add_f32 v[4:5], v[4:5], v[8:9]
	s_waitcnt vmcnt(1)
	v_pk_add_f32 v[10:11], v[12:13], v[16:17]
	s_nop 0
	v_pk_add_f32 v[10:11], v[4:5], v[10:11]
	v_pk_add_f32 v[8:9], v[14:15], v[18:19]
	v_pk_add_f32 v[8:9], v[6:7], v[8:9]
	v_add_u32_e32 v0, s18, v0
	v_cmp_lt_i32_e32 vcc, s0, v0
	s_or_b64 s[16:17], vcc, s[16:17]
	s_waitcnt vmcnt(0)
	v_pk_add_f32 v[4:5], v[22:23], v[10:11]
	s_nop 0
	v_mul_f32_e32 v2, 0x3d372713, v4
	v_mul_f32_e32 v2, v4, v2
	v_fma_f32 v2, v4, v2, v4
	v_mul_f32_e32 v2, 0xbfcc422a, v2
	v_mul_f32_e32 v2, 0x3fb8aa3b, v2
	v_exp_f32_e32 v2, v2
	v_pk_add_f32 v[6:7], v[24:25], v[8:9]
	v_add_f32_e32 v2, 1.0, v2
	v_rcp_f32_e32 v2, v2
	s_nop 0
	v_mul_f32_e32 v2, v4, v2
	v_mul_f32_e32 v4, 0x3d372713, v5
	v_mul_f32_e32 v4, v5, v4
	v_fma_f32 v4, v5, v4, v5
	v_mul_f32_e32 v4, 0xbfcc422a, v4
	v_mul_f32_e32 v4, 0x3fb8aa3b, v4
	v_exp_f32_e32 v4, v4
	s_nop 0
	v_add_f32_e32 v4, 1.0, v4
	v_rcp_f32_e32 v4, v4
	s_nop 0
	v_mul_f32_e32 v4, v5, v4
	v_cvt_pk_bf16_f32 v4, v2, v4
	v_mul_f32_e32 v2, 0x3d372713, v6
	v_mul_f32_e32 v5, 0x3d372713, v7
	v_mul_f32_e32 v2, v6, v2
	v_mul_f32_e32 v5, v7, v5
	v_fma_f32 v2, v6, v2, v6
	v_fma_f32 v5, v7, v5, v7
	v_mul_f32_e32 v2, 0xbfcc422a, v2
	v_mul_f32_e32 v5, 0xbfcc422a, v5
	v_mul_f32_e32 v2, 0x3fb8aa3b, v2
	v_mul_f32_e32 v5, 0x3fb8aa3b, v5
	v_exp_f32_e32 v2, v2
	v_exp_f32_e32 v5, v5
	v_add_f32_e32 v2, 1.0, v2
	v_add_f32_e32 v5, 1.0, v5
	v_rcp_f32_e32 v2, v2
	v_rcp_f32_e32 v5, v5
	v_mul_f32_e32 v2, v6, v2
	v_mul_f32_e32 v5, v7, v5
	v_lshl_add_u64 v[6:7], v[20:21], 1, s[2:3]
	v_cvt_pk_bf16_f32 v5, v2, v5
	global_store_dwordx2 v[6:7], v[4:5], off
	s_andn2_b64 exec, exec, s[16:17]
	s_cbranch_execnz .LBB0_2210
